# P6 cooperative L2 touch of the act panel one K-iteration ahead of its LDS-DMA (four sharers each touch a quarter of the rows), on top of nt loads + reversed P6
# speedup vs baseline: 1.0061x; 1.0023x over previous
; template <class Epi, class Sched>
; __device__ __forceinline__ void gemm_phase(LAS unsigned char* lds, const Sched& S, const Epi& E, const int wid) {
;     ...
;         for (int t = 0; t < nt; t += 2) {
;             const bool last = (t == nt - 2);
;             const char* a1 = cA + (size_t)(t + 1) * kstep;
;             const char* a2 = last ? nA : cA + (size_t)(t + 2) * kstep; const char* b2 = last ? nB : cB + (size_t)(t + 2) * kstep;
;             const char* a3 = a2 + kstep; const char* b3 = b2 + kstep;
.LBB7_869:
	s_cmp_gt_u32 s94, 1
	s_cbranch_scc1 .Lp6_notouch
	s_sub_i32 s100, s81, 2
	s_lshl_b32 s100, s100, 7
	s_cmp_gt_i32 s81, 0
	s_cselect_b32 s98, s41, s42
	s_cselect_b32 s99, s21, s43
	s_cselect_b32 s100, s100, 0x200
	s_add_u32 s98, s98, s100
	s_addc_u32 s99, s99, 0
	s_lshl_b32 s100, s94, 7
	s_add_u32 s98, s98, s100
	s_addc_u32 s99, s99, 0
	s_and_b32 s100, s95, 3
	s_lshl_b32 s100, s100, 6
	v_mbcnt_lo_u32_b32 v255, -1, 0
	v_mbcnt_hi_u32_b32 v255, -1, v255
	v_add_u32_e32 v255, s100, v255
	v_lshlrev_b32_e32 v255, 10, v255
	global_load_dword v255, v255, s[98:99]
